# speedup vs baseline: 1.0427x; 1.0120x over previous
_Z11lstm_kernelPKiPKhPKfS4_S4_Pf:
	s_load_dwordx4 s[12:15], s[0:1], 0x0
	v_readfirstlane_b32 s19, v0
	v_or_b32_e32 v3, 0x400, v0
	s_movk_i32 s4, 0x500
	s_lshr_b32 s7, s19, 6
	s_lshl_b32 s18, s2, 6
	s_mulk_i32 s2, 0x1400
	v_mov_b32_e32 v2, 0x4ff
	v_cmp_gt_u32_e32 vcc, s4, v3
	s_mul_hi_i32 s3, s18, 0x50
	s_waitcnt lgkmcnt(0)
	s_add_u32 s2, s12, s2
	v_cndmask_b32_e32 v2, v2, v3, vcc
	s_addc_u32 s3, s13, s3
	v_lshlrev_b32_e32 v1, 2, v0
	v_lshlrev_b32_e32 v4, 2, v2
	s_movk_i32 s4, 0x184
	v_or_b32_e32 v28, 0x200, v0
	global_load_dword v29, v1, s[2:3]
	global_load_dword v30, v1, s[2:3] offset:2048
	global_load_dword v2, v4, s[2:3]
	v_mov_b32_e32 v4, 0x383
	v_cmp_gt_u32_e32 vcc, s4, v0
	s_add_u32 s2, s14, 0x34000
	s_addc_u32 s3, s15, 0
	v_cndmask_b32_e32 v4, v4, v28, vcc
	v_lshlrev_b32_e32 v31, 4, v0
	v_lshlrev_b32_e32 v4, 4, v4
	global_load_dwordx4 v[6:9], v31, s[2:3]
	global_load_dwordx4 v[10:13], v4, s[2:3]
	v_and_b32_e32 v4, 0x7f, v0
	v_lshlrev_b32_e32 v18, 4, v4
	v_mov_b32_e32 v19, 0
	v_lshl_add_u64 v[4:5], s[14:15], 0, v[18:19]
	s_mov_b32 s2, 0x37000
	v_add_co_u32_e64 v4, s[2:3], s2, v4
	s_nop 1
	v_addc_co_u32_e64 v5, s[2:3], 0, v5, s[2:3]
	global_load_dwordx4 v[14:17], v[4:5], off offset:2112
	s_movk_i32 s22, 0x410
	s_movk_i32 s2, 0x4ff
	v_and_b32_e32 v4, 63, v0
	v_cmp_lt_u32_e64 s[2:3], s2, v3
	s_mul_i32 s5, s7, 0x6000
	s_mul_hi_u32 s4, s7, 0x6000
	s_add_u32 s8, s14, s5
	s_addc_u32 s9, s15, s4
	v_lshlrev_b32_e32 v210, 4, v4
	v_mov_b32_e32 v211, v19
	v_lshl_add_u64 v[20:21], s[8:9], 0, v[210:211]
	s_movk_i32 s4, 0x2000
	v_add_co_u32_e64 v22, s[4:5], s4, v20
	s_nop 1
	v_addc_co_u32_e64 v23, s[4:5], 0, v21, s[4:5]
	s_movk_i32 s4, 0x3000
	s_nop 0
	v_add_co_u32_e64 v24, s[4:5], s4, v20
	global_load_dwordx4 v[90:93], v[22:23], off offset:1024
	global_load_dwordx4 v[86:89], v[22:23], off offset:2048
	v_addc_co_u32_e64 v25, s[4:5], 0, v21, s[4:5]
	s_movk_i32 s4, 0x5000
	s_nop 0
	v_add_co_u32_e64 v26, s[4:5], s4, v20
	s_nop 1
	v_addc_co_u32_e64 v27, s[4:5], 0, v21, s[4:5]
	global_load_dwordx4 v[82:85], v[22:23], off offset:3072
	global_load_dwordx4 v[46:49], v[26:27], off
	global_load_dwordx4 v[42:45], v[26:27], off offset:1024
	global_load_dwordx4 v[38:41], v[26:27], off offset:2048
	global_load_dwordx4 v[94:97], v[24:25], off offset:-4096
	global_load_dwordx4 v[34:37], v[26:27], off offset:3072
	s_movk_i32 s4, 0x1000
	v_add_co_u32_e64 v22, s[4:5], s4, v20
	global_load_dwordx4 v[126:129], v210, s[8:9]
	global_load_dwordx4 v[122:125], v210, s[8:9] offset:1024
	global_load_dwordx4 v[118:121], v210, s[8:9] offset:2048
	global_load_dwordx4 v[114:117], v210, s[8:9] offset:3072
	v_addc_co_u32_e64 v23, s[4:5], 0, v21, s[4:5]
	global_load_dwordx4 v[110:113], v[22:23], off
	global_load_dwordx4 v[106:109], v[22:23], off offset:1024
	global_load_dwordx4 v[102:105], v[22:23], off offset:2048
	global_load_dwordx4 v[98:101], v[22:23], off offset:3072
	global_load_dwordx4 v[78:81], v[24:25], off
	global_load_dwordx4 v[74:77], v[24:25], off offset:1024
	global_load_dwordx4 v[70:73], v[24:25], off offset:2048
	global_load_dwordx4 v[66:69], v[24:25], off offset:3072
	s_movk_i32 s4, 0x4000
	v_add_co_u32_e64 v20, s[4:5], s4, v20
	v_mov_b32_e32 v5, 0x4000
	s_nop 0
	v_addc_co_u32_e64 v21, s[4:5], 0, v21, s[4:5]
	global_load_dwordx4 v[62:65], v[20:21], off
	global_load_dwordx4 v[58:61], v[20:21], off offset:1024
	global_load_dwordx4 v[54:57], v[20:21], off offset:2048
	global_load_dwordx4 v[50:53], v[20:21], off offset:3072
	s_waitcnt vmcnt(26)
	ds_write_b128 v31, v[6:9] offset:16384
	v_lshl_or_b32 v5, v28, 4, v5
	v_add_u32_e32 v6, 0x9840, v31
	v_cndmask_b32_e32 v5, v6, v5, vcc
	s_waitcnt vmcnt(25)
	ds_write_b128 v5, v[10:13]
	s_waitcnt vmcnt(24)
	ds_write_b128 v18, v[14:17] offset:36928
	v_mul_u32_u24_e32 v5, 0xccd, v0
	v_lshrrev_b32_e32 v5, 16, v5
	s_mov_b32 s5, 0xffffec
	v_mul_u32_u24_e32 v6, 0xccd, v28
	s_movk_i32 s4, 0x90
	v_mad_u32_u24 v8, v5, s5, v0
	v_lshlrev_b32_e32 v5, 2, v5
	v_lshrrev_b32_e32 v6, 16, v6
	v_mul_lo_u32 v7, v29, s4
	v_lshl_or_b32 v5, v8, 8, v5
	ds_write_b32 v5, v7 offset:30784
	v_mul_lo_u32 v196, v29, s22
	v_add_u32_e32 v197, 0x24e80, v5
	ds_write_b32 v197, v196
	v_mad_u32_u24 v7, v6, s5, v28
	v_lshlrev_b32_e32 v6, 2, v6
	v_mul_lo_u32 v5, v30, s4
	v_lshl_or_b32 v6, v7, 8, v6
	ds_write_b32 v6, v5 offset:30784
	v_mul_lo_u32 v198, v30, s22
	v_add_u32_e32 v199, 0x24e80, v6
	ds_write_b32 v199, v198
	s_and_saveexec_b64 s[4:5], s[2:3]
	s_xor_b64 s[2:3], exec, s[4:5]
	v_mov_b32_e32 v3, 0x9840
	v_lshl_add_u32 v5, v0, 2, v3
	s_andn2_saveexec_b64 s[2:3], s[2:3]
	v_mul_u32_u24_e32 v5, 0xccd, v3
	s_mov_b32 s4, 0xffffec
	v_mul_u32_u24_sdwa v6, v5, s4 dst_sel:DWORD dst_unused:UNUSED_PAD src0_sel:WORD_1 src1_sel:DWORD
	v_add_lshl_u32 v3, v6, v3, 8
	v_mov_b32_e32 v6, 2
	v_lshlrev_b32_sdwa v5, v6, v5 dst_sel:DWORD dst_unused:UNUSED_PAD src0_sel:DWORD src1_sel:WORD_1
	s_movk_i32 s4, 0x7840
	v_add3_u32 v5, v5, v3, s4
	s_or_b64 exec, exec, s[2:3]
	v_lshrrev_b32_e32 v3, 5, v4
	s_movk_i32 s2, 0x90
	s_lshl_b32 s6, s7, 10
	s_mulk_i32 s7, 0xfd00
	v_and_b32_e32 v182, 31, v0
	v_mul_lo_u32 v200, v2, s22
	v_mul_lo_u32 v2, v2, s2
	s_add_i32 s7, s6, s7
	v_lshlrev_b32_e32 v229, 6, v3
	ds_write_b32 v5, v2
	v_add_u32_e32 v201, 0x1d640, v5
	ds_write_b32 v201, v200
	v_lshlrev_b32_e32 v230, 4, v3
	v_lshlrev_b32_e32 v228, 2, v182
	v_or_b32_e32 v2, s7, v229
	v_mov_b32_e32 v204, 0
	v_mov_b32_e32 v205, 0
	v_mov_b32_e32 v206, 0
	v_mov_b32_e32 v207, 0
	ds_write_b128 v31, v[204:207]
	ds_write_b128 v31, v[204:207] offset:8192
	v_and_b32_e32 v202, 0xfc, v1
	v_add_u32_e32 v202, 0x26280, v202
	ds_write_b32 v202, v204
	s_waitcnt lgkmcnt(0)
	s_barrier
	s_cmpk_lt_u32 s19, 0x100
	s_cbranch_scc1 .Llight_path
	s_setprio 1
	v_add_u32_e32 v3, 0x7800, v228
	ds_read2_b32 v[138:139], v3 offset0:16 offset1:48
	ds_read_b128 v[18:21], v2 offset:36928
	ds_read_b128 v[22:25], v2 offset:36944
	s_waitcnt lgkmcnt(2)
	v_add_u32_e32 v3, v230, v138
	ds_read_b128 v[26:29], v2 offset:36960
	ds_read_b128 v[30:33], v2 offset:36976
	ds_read_b128 v[142:145], v3 offset:16384
	ds_read_b128 v[130:133], v3 offset:16416
	ds_read_b128 v[154:157], v3 offset:16448
	ds_read_b128 v[134:137], v3 offset:16480
	ds_read_b128 v[14:17], v2 offset:37104
	ds_read_b128 v[10:13], v2 offset:37088
	ds_read_b128 v[6:9], v2 offset:37072
	ds_read_b128 v[2:5], v2 offset:37056
	s_waitcnt vmcnt(17) lgkmcnt(7)
	v_mfma_f32_32x32x16_bf16 v[18:33], v[94:97], v[142:145], v[18:33]
	s_waitcnt lgkmcnt(6)
	v_mfma_f32_32x32x16_bf16 v[18:33], v[90:93], v[130:133], v[18:33]
	s_waitcnt lgkmcnt(5)
	v_mfma_f32_32x32x16_bf16 v[18:33], v[86:89], v[154:157], v[18:33]
	s_waitcnt lgkmcnt(4)
	v_mfma_f32_32x32x16_bf16 v[18:33], v[82:85], v[134:137], v[18:33]
	s_cmpk_lt_u32 s19, 0x100
	s_cselect_b64 s[2:3], -1, 0
	ds_read_b32 v158, v228 offset:31040
	v_add_u32_e32 v159, v230, v139
	s_nop 2
	v_exp_f32_e32 v139, v20
	v_exp_f32_e32 v138, v24
	v_exp_f32_e32 v141, v28
	v_exp_f32_e32 v140, v32
	v_exp_f32_e32 v18, v18
	v_exp_f32_e32 v20, v22
	v_exp_f32_e32 v22, v26
	v_add_f32_e32 v24, 1.0, v138
	v_add_f32_e32 v26, 1.0, v141
	v_add_f32_e32 v19, 1.0, v139
	v_exp_f32_e32 v23, v30
	v_add_f32_e32 v27, 1.0, v140
	v_fmac_f32_e32 v24, v20, v24
	v_fmac_f32_e32 v26, v22, v26
	v_fmac_f32_e32 v19, v18, v19
	v_fmac_f32_e32 v27, v23, v27
	v_rcp_f32_e32 v18, v24
	v_rcp_f32_e32 v22, v27
	v_rcp_f32_e32 v19, v19
	v_rcp_f32_e32 v23, v26
	v_exp_f32_e32 v146, v21
	v_exp_f32_e32 v147, v25
	s_mov_b32 s8, 0xc038aa3b
	s_mov_b32 s4, 0x4038aa3b
	v_mov_b64_e32 v[160:161], s[8:9]
	v_exp_f32_e32 v148, v29
	v_exp_f32_e32 v149, v33
	v_pk_fma_f32 v[20:21], v[138:139], s[4:5], v[160:161] op_sel_hi:[1,0,0]
	s_nop 0
	v_pk_mul_f32 v[214:215], v[20:21], v[18:19]
	v_pk_fma_f32 v[18:19], v[140:141], s[4:5], v[160:161] op_sel_hi:[1,0,0]
	s_nop 0
	v_pk_mul_f32 v[212:213], v[18:19], v[22:23]
	v_add_u32_e32 v231, s7, v229
	ds_read_b128 v[18:21], v231 offset:36928
	ds_read_b128 v[22:25], v231 offset:36944
	ds_read_b128 v[26:29], v231 offset:36960
	ds_read_b128 v[30:33], v231 offset:36976
	s_waitcnt lgkmcnt(5)
	v_mfma_f32_32x32x16_bf16 v[2:17], v[46:49], v[142:145], v[2:17]
	ds_read_b128 v[138:141], v159 offset:16384
	v_add_f32_e32 v162, 1.0, v146
	v_exp_f32_e32 v163, v215
	v_exp_f32_e32 v164, v214
	v_exp_f32_e32 v165, v213
	v_exp_f32_e32 v166, v212
	v_add_f32_e32 v142, 1.0, v147
	v_add_f32_e32 v143, 1.0, v148
	v_add_f32_e32 v144, 1.0, v149
	v_mfma_f32_32x32x16_bf16 v[2:17], v[42:45], v[130:133], v[2:17]
	ds_read_b128 v[146:149], v159 offset:16416
	v_fmac_f32_e32 v162, v162, v163
	v_fmac_f32_e32 v142, v142, v164
	v_fmac_f32_e32 v143, v143, v165
	v_fmac_f32_e32 v144, v144, v166
	v_mfma_f32_32x32x16_bf16 v[2:17], v[38:41], v[154:157], v[2:17]
	ds_read_b128 v[150:153], v159 offset:16448
	v_rcp_f32_e32 v130, v162
	v_rcp_f32_e32 v131, v142
	v_rcp_f32_e32 v132, v143
	v_rcp_f32_e32 v133, v144
	s_waitcnt vmcnt(16)
	v_mfma_f32_32x32x16_bf16 v[2:17], v[34:37], v[134:137], v[2:17]
	ds_read_b128 v[178:181], v159 offset:16480
	v_fma_f32 v130, -v163, v130, v130
	v_fma_f32 v131, -v164, v131, v131
	v_fma_f32 v132, -v165, v132, v132
	v_fma_f32 v133, -v166, v133, v133
	v_add_u32_e32 v211, s6, v210
	v_cvt_pk_bf16_f32 v130, v130, v131
	v_cvt_pk_bf16_f32 v131, v132, v133
	ds_write_b64 v211, v[130:131]
	s_nop 3
	v_exp_f32_e32 v131, v4
	v_exp_f32_e32 v130, v8
	v_exp_f32_e32 v133, v12
	v_exp_f32_e32 v132, v16
	v_exp_f32_e32 v2, v2
	v_exp_f32_e32 v4, v6
	v_exp_f32_e32 v6, v10
	v_exp_f32_e32 v7, v14
	v_add_f32_e32 v3, 1.0, v131
	v_add_f32_e32 v8, 1.0, v130
	v_add_f32_e32 v10, 1.0, v133
	v_add_f32_e32 v11, 1.0, v132
	v_fmac_f32_e32 v3, v2, v3
	v_fmac_f32_e32 v8, v4, v8
	v_fmac_f32_e32 v10, v6, v10
	v_fmac_f32_e32 v11, v7, v11
	v_rcp_f32_e32 v3, v3
	v_rcp_f32_e32 v2, v8
	v_rcp_f32_e32 v7, v10
	v_rcp_f32_e32 v6, v11
	v_exp_f32_e32 v134, v5
	v_exp_f32_e32 v135, v9
	v_pk_fma_f32 v[4:5], v[130:131], s[4:5], v[160:161] op_sel_hi:[1,0,0]
	v_exp_f32_e32 v130, v13
	v_pk_mul_f32 v[204:205], v[4:5], v[2:3]
	v_pk_fma_f32 v[2:3], v[132:133], s[4:5], v[160:161] op_sel_hi:[1,0,0]
	v_exp_f32_e32 v131, v17
	v_pk_mul_f32 v[202:203], v[2:3], v[6:7]
	ds_read_b128 v[2:5], v231 offset:37056
	ds_read_b128 v[6:9], v231 offset:37072
	ds_read_b128 v[10:13], v231 offset:37088
	ds_read_b128 v[14:17], v231 offset:37104
	s_waitcnt lgkmcnt(8)
	v_mfma_f32_32x32x16_bf16 v[18:33], v[94:97], v[138:141], v[18:33]
	v_add_f32_e32 v132, 1.0, v134
	v_exp_f32_e32 v133, v205
	v_add_f32_e32 v134, 1.0, v135
	v_exp_f32_e32 v135, v204
	v_exp_f32_e32 v136, v203
	v_exp_f32_e32 v137, v202
	v_add_f32_e32 v130, 1.0, v130
	v_add_f32_e32 v131, 1.0, v131
	s_waitcnt lgkmcnt(7)
	v_mfma_f32_32x32x16_bf16 v[18:33], v[90:93], v[146:149], v[18:33]
	v_fmac_f32_e32 v132, v132, v133
	v_fmac_f32_e32 v134, v134, v135
	v_fmac_f32_e32 v130, v130, v136
	v_fmac_f32_e32 v131, v131, v137
	s_waitcnt lgkmcnt(6)
	v_mfma_f32_32x32x16_bf16 v[18:33], v[86:89], v[150:153], v[18:33]
	v_rcp_f32_e32 v132, v132
	v_rcp_f32_e32 v134, v134
	v_rcp_f32_e32 v130, v130
	v_rcp_f32_e32 v131, v131
	s_waitcnt lgkmcnt(5)
	v_mfma_f32_32x32x16_bf16 v[18:33], v[82:85], v[178:181], v[18:33]
	v_fma_f32 v132, -v133, v132, v132
	v_fma_f32 v133, -v135, v134, v134
	v_fma_f32 v134, -v136, v130, v130
	v_fma_f32 v131, -v137, v131, v131
	v_cvt_pk_bf16_f32 v130, v132, v133
	v_cvt_pk_bf16_f32 v131, v134, v131
	ds_write_b64 v211, v[130:131] offset:8
	s_waitcnt lgkmcnt(0)
	s_barrier
	s_load_dwordx8 s[4:11], s[0:1], 0x10
	ds_read_b32 v194, v228 offset:31168
	ds_read_b128 v[174:177], v210
	v_add_u32_e32 v183, v230, v158
	ds_read_b128 v[170:173], v210 offset:1024
	v_exp_f32_e32 v131, v20
	v_exp_f32_e32 v130, v24
	v_exp_f32_e32 v133, v28
	v_exp_f32_e32 v132, v32
	ds_read_b128 v[166:169], v210 offset:2048
	v_exp_f32_e32 v18, v18
	v_exp_f32_e32 v20, v22
	v_exp_f32_e32 v22, v26
	v_exp_f32_e32 v23, v30
	v_add_f32_e32 v19, 1.0, v131
	v_add_f32_e32 v24, 1.0, v130
	v_add_f32_e32 v26, 1.0, v133
	v_add_f32_e32 v27, 1.0, v132
	ds_read_b128 v[162:165], v210 offset:3072
	v_fmac_f32_e32 v19, v18, v19
	v_fmac_f32_e32 v24, v20, v24
	v_fmac_f32_e32 v26, v22, v26
	v_fmac_f32_e32 v27, v23, v27
	ds_read_b128 v[158:161], v210 offset:4096
	v_rcp_f32_e32 v19, v19
	v_rcp_f32_e32 v18, v24
	v_rcp_f32_e32 v23, v26
	v_rcp_f32_e32 v22, v27
	ds_read_b128 v[154:157], v210 offset:5120
	v_exp_f32_e32 v186, v21
	v_exp_f32_e32 v187, v25
	ds_read_b128 v[142:145], v210 offset:6144
	s_mov_b32 s0, 0xc038aa3b
	s_mov_b32 s12, 0x4038aa3b
	v_mov_b64_e32 v[184:185], s[0:1]
	v_pk_fma_f32 v[20:21], v[130:131], s[12:13], v[184:185] op_sel_hi:[1,0,0]
	v_exp_f32_e32 v188, v29
	v_pk_mul_f32 v[200:201], v[20:21], v[18:19]
	v_pk_fma_f32 v[18:19], v[132:133], s[12:13], v[184:185] op_sel_hi:[1,0,0]
	v_exp_f32_e32 v189, v33
	v_pk_mul_f32 v[198:199], v[18:19], v[22:23]
	ds_read_b128 v[130:133], v210 offset:7168
	ds_read_b128 v[18:21], v231 offset:36928
	ds_read_b128 v[22:25], v231 offset:36944
	ds_read_b128 v[26:29], v231 offset:36960
	ds_read_b128 v[30:33], v231 offset:36976
	v_mfma_f32_32x32x16_bf16 v[2:17], v[46:49], v[138:141], v[2:17]
	ds_read_b128 v[134:137], v183 offset:16384
	v_add_f32_e32 v186, 1.0, v186
	v_exp_f32_e32 v190, v201
	v_exp_f32_e32 v191, v200
	v_exp_f32_e32 v192, v199
	v_exp_f32_e32 v193, v198
	v_add_f32_e32 v187, 1.0, v187
	v_add_f32_e32 v188, 1.0, v188
	v_add_f32_e32 v189, 1.0, v189
	v_mfma_f32_32x32x16_bf16 v[2:17], v[42:45], v[146:149], v[2:17]
	ds_read_b128 v[138:141], v183 offset:16416
	v_fmac_f32_e32 v186, v186, v190
	v_fmac_f32_e32 v187, v187, v191
	v_fmac_f32_e32 v188, v188, v192
	v_fmac_f32_e32 v189, v189, v193
	v_mfma_f32_32x32x16_bf16 v[2:17], v[38:41], v[150:153], v[2:17]
	ds_read_b128 v[146:149], v183 offset:16448
	v_rcp_f32_e32 v186, v186
	v_rcp_f32_e32 v187, v187
	v_rcp_f32_e32 v188, v188
	v_rcp_f32_e32 v189, v189
	v_mfma_f32_32x32x16_bf16 v[2:17], v[34:37], v[178:181], v[2:17]
	ds_read_b128 v[150:153], v183 offset:16480
	v_fma_f32 v183, -v190, v186, v186
	v_fma_f32 v186, -v191, v187, v187
	v_fma_f32 v187, -v192, v188, v188
	v_fma_f32 v188, -v193, v189, v189
	s_waitcnt vmcnt(15) lgkmcnt(0)
	v_mfma_f32_32x32x16_bf16 v[18:33], v[126:129], v[174:177], v[18:33]
	v_cvt_pk_bf16_f32 v178, v183, v186
	v_cvt_pk_bf16_f32 v179, v187, v188
	ds_write_b64 v211, v[178:179] offset:8192
	s_waitcnt vmcnt(14)
	v_mfma_f32_32x32x16_bf16 v[18:33], v[122:125], v[170:173], v[18:33]
	s_nop 0
	v_exp_f32_e32 v179, v4
	v_exp_f32_e32 v178, v8
	v_exp_f32_e32 v181, v12
	v_exp_f32_e32 v180, v16
	s_waitcnt vmcnt(13)
	v_mfma_f32_32x32x16_bf16 v[18:33], v[118:121], v[166:169], v[18:33]
	v_exp_f32_e32 v2, v2
	v_exp_f32_e32 v4, v6
	v_exp_f32_e32 v7, v10
	v_exp_f32_e32 v8, v14
	v_add_f32_e32 v3, 1.0, v179
	v_add_f32_e32 v6, 1.0, v178
	v_add_f32_e32 v10, 1.0, v181
	v_add_f32_e32 v11, 1.0, v180
	s_waitcnt vmcnt(12)
	v_mfma_f32_32x32x16_bf16 v[18:33], v[114:117], v[162:165], v[18:33]
	v_fmac_f32_e32 v3, v2, v3
	v_fmac_f32_e32 v6, v4, v6
	v_fmac_f32_e32 v10, v7, v10
	v_fmac_f32_e32 v11, v8, v11
	s_waitcnt vmcnt(11)
	v_mfma_f32_32x32x16_bf16 v[18:33], v[110:113], v[158:161], v[18:33]
	v_rcp_f32_e32 v3, v3
	v_rcp_f32_e32 v2, v6
	v_rcp_f32_e32 v7, v10
	v_rcp_f32_e32 v6, v11
	s_waitcnt vmcnt(10)
	v_mfma_f32_32x32x16_bf16 v[18:33], v[106:109], v[154:157], v[18:33]
	v_exp_f32_e32 v183, v5
	v_exp_f32_e32 v186, v9
	s_waitcnt vmcnt(9)
	v_mfma_f32_32x32x16_bf16 v[18:33], v[102:105], v[142:145], v[18:33]
	v_fma_f32 v4, v178, s12, v184
	v_fma_f32 v5, v179, s12, v184
	v_exp_f32_e32 v178, v13
	v_pk_mul_f32 v[206:207], v[4:5], v[2:3]
	v_pk_fma_f32 v[2:3], v[180:181], s[12:13], v[184:185] op_sel_hi:[1,0,0]
	v_exp_f32_e32 v179, v17
	v_pk_mul_f32 v[208:209], v[2:3], v[6:7]
	s_waitcnt vmcnt(8)
	v_mfma_f32_32x32x16_bf16 v[18:33], v[98:101], v[130:133], v[18:33]
	ds_read_b128 v[2:5], v231 offset:37056
	ds_read_b128 v[6:9], v231 offset:37072
	ds_read_b128 v[10:13], v231 offset:37088
	ds_read_b128 v[14:17], v231 offset:37104
	v_mfma_f32_32x32x16_bf16 v[18:33], v[94:97], v[134:137], v[18:33]
	v_add_f32_e32 v180, 1.0, v183
	v_exp_f32_e32 v181, v207
	v_add_f32_e32 v183, 1.0, v186
	v_exp_f32_e32 v184, v206
	v_exp_f32_e32 v185, v209
	v_exp_f32_e32 v186, v208
	v_add_f32_e32 v178, 1.0, v178
	v_add_f32_e32 v179, 1.0, v179
	v_mfma_f32_32x32x16_bf16 v[18:33], v[90:93], v[138:141], v[18:33]
	v_fmac_f32_e32 v180, v180, v181
	v_fmac_f32_e32 v183, v183, v184
	v_fmac_f32_e32 v178, v178, v185
	v_fmac_f32_e32 v179, v179, v186
	v_mfma_f32_32x32x16_bf16 v[18:33], v[86:89], v[146:149], v[18:33]
	v_rcp_f32_e32 v180, v180
	v_rcp_f32_e32 v183, v183
	v_rcp_f32_e32 v178, v178
	v_rcp_f32_e32 v179, v179
	v_mfma_f32_32x32x16_bf16 v[18:33], v[82:85], v[150:153], v[18:33]
	v_fma_f32 v180, -v181, v180, v180
	v_fma_f32 v181, -v184, v183, v183
	v_fma_f32 v183, -v185, v178, v178
	v_fma_f32 v179, -v186, v179, v179
	v_cvt_pk_bf16_f32 v178, v180, v181
	v_cvt_pk_bf16_f32 v179, v183, v179
	ds_write_b64 v211, v[178:179] offset:8200
	s_waitcnt lgkmcnt(0)
	s_barrier
	v_mov_b32_e32 v178, 0x7a40
	v_lshl_add_u32 v232, v182, 2, v178
	s_mov_b32 s1, -1
	s_branch .LBB1_14

.LBB1_14:
	s_waitcnt vmcnt(7)
	v_mfma_f32_32x32x16_bf16 v[2:17], v[78:81], v[174:177], v[2:17]
	v_add_u32_e32 v192, v230, v194
	ds_read_b32 v216, v232
	ds_read_b128 v[194:197], v210 offset:8192
	s_waitcnt vmcnt(6)
	v_mfma_f32_32x32x16_bf16 v[2:17], v[74:77], v[170:173], v[2:17]
	ds_read_b128 v[178:181], v210 offset:9216
	v_exp_f32_e32 v187, v20
	v_exp_f32_e32 v186, v24
	v_exp_f32_e32 v189, v28
	v_exp_f32_e32 v188, v32
	s_waitcnt vmcnt(5)
	v_mfma_f32_32x32x16_bf16 v[2:17], v[70:73], v[166:169], v[2:17]
	ds_read_b128 v[170:173], v210 offset:10240
	v_exp_f32_e32 v18, v18
	v_exp_f32_e32 v22, v22
	v_exp_f32_e32 v24, v26
	v_exp_f32_e32 v26, v30
	v_add_f32_e32 v20, 1.0, v187
	v_add_f32_e32 v28, 1.0, v186
	v_add_f32_e32 v30, 1.0, v189
	v_add_f32_e32 v32, 1.0, v188
	s_waitcnt vmcnt(4)
	v_mfma_f32_32x32x16_bf16 v[2:17], v[66:69], v[162:165], v[2:17]
	ds_read_b128 v[166:169], v210 offset:11264
	v_exp_f32_e32 v19, v19
	v_exp_f32_e32 v23, v23
	v_exp_f32_e32 v27, v27
	v_exp_f32_e32 v31, v31
	v_fmac_f32_e32 v20, v18, v20
	v_fmac_f32_e32 v28, v22, v28
	v_fmac_f32_e32 v30, v24, v30
	v_fmac_f32_e32 v32, v26, v32
	s_waitcnt vmcnt(3)
	v_mfma_f32_32x32x16_bf16 v[2:17], v[62:65], v[158:161], v[2:17]
	ds_read_b128 v[162:165], v210 offset:12288
	v_add_f32_e32 v22, 1.0, v19
	v_rcp_f32_e32 v19, v20
	v_rcp_f32_e32 v18, v28
	v_rcp_f32_e32 v191, v30
	v_rcp_f32_e32 v190, v32
	v_add_f32_e32 v20, 1.0, v23
	s_waitcnt vmcnt(2)
	v_mfma_f32_32x32x16_bf16 v[2:17], v[58:61], v[154:157], v[2:17]
	ds_read_b128 v[174:177], v210 offset:13312
	v_rcp_f32_e32 v159, v22
	v_rcp_f32_e32 v158, v20
	v_exp_f32_e32 v160, v21
	v_exp_f32_e32 v161, v25
	v_add_f32_e32 v23, 1.0, v27
	v_add_f32_e32 v20, 1.0, v31
	s_waitcnt vmcnt(1)
	v_mfma_f32_32x32x16_bf16 v[2:17], v[54:57], v[142:145], v[2:17]
	ds_read_b128 v[182:185], v210 offset:14336
	v_rcp_f32_e32 v155, v23
	v_rcp_f32_e32 v154, v20
	v_exp_f32_e32 v193, v29
	v_exp_f32_e32 v217, v33
	s_waitcnt vmcnt(0)
	v_mfma_f32_32x32x16_bf16 v[2:17], v[50:53], v[130:133], v[2:17]
	v_mov_b64_e32 v[218:219], s[0:1]
	v_fma_f32 v20, v186, s12, v218
	v_fma_f32 v21, v187, s12, v218
	ds_read_b128 v[142:145], v210 offset:15360
	v_mul_f32_e64 v156, v20, v18
	v_mul_f32_e64 v157, v21, v19
	ds_read_b128 v[18:21], v231 offset:36928
	ds_read_b128 v[22:25], v231 offset:36944
	ds_read_b128 v[26:29], v231 offset:36960
	ds_read_b128 v[30:33], v231 offset:36976
	v_pk_fma_f32 v[130:131], v[188:189], s[12:13], v[218:219] op_sel_hi:[1,0,0]
	v_pk_fma_f32 v[214:215], v[158:159], v[214:215], v[156:157]
	v_pk_mul_f32 v[130:131], v[130:131], v[190:191]
	s_nop 0
	v_pk_fma_f32 v[212:213], v[154:155], v[212:213], v[130:131]
	v_mfma_f32_32x32x16_bf16 v[2:17], v[46:49], v[134:137], v[2:17]
	ds_read_b128 v[154:157], v192 offset:16384
	v_add_f32_e32 v130, 1.0, v160
	v_exp_f32_e32 v131, v215
	v_exp_f32_e32 v132, v214
	v_exp_f32_e32 v133, v213
	v_exp_f32_e32 v220, v212
	v_add_f32_e32 v134, 1.0, v161
	v_add_f32_e32 v135, 1.0, v193
	v_add_f32_e32 v136, 1.0, v217
	v_mfma_f32_32x32x16_bf16 v[2:17], v[42:45], v[138:141], v[2:17]
	ds_read_b128 v[158:161], v192 offset:16416
	v_fmac_f32_e32 v130, v130, v131
	v_fmac_f32_e32 v134, v134, v132
	v_fmac_f32_e32 v135, v135, v133
	v_fmac_f32_e32 v136, v136, v220
	v_mfma_f32_32x32x16_bf16 v[2:17], v[38:41], v[146:149], v[2:17]
	ds_read_b128 v[186:189], v192 offset:16448
	v_rcp_f32_e32 v130, v130
	v_rcp_f32_e32 v134, v134
	v_rcp_f32_e32 v135, v135
	v_rcp_f32_e32 v136, v136
	v_mfma_f32_32x32x16_bf16 v[2:17], v[34:37], v[150:153], v[2:17]
	ds_read_b128 v[190:193], v192 offset:16480
	v_fma_f32 v130, -v131, v130, v130
	v_fma_f32 v131, -v132, v134, v134
	v_fma_f32 v132, -v133, v135, v135
	v_fma_f32 v133, -v220, v136, v136
	s_waitcnt lgkmcnt(4)
	v_mfma_f32_32x32x16_bf16 v[18:33], v[126:129], v[194:197], v[18:33]
	v_cvt_pk_bf16_f32 v130, v130, v131
	v_cvt_pk_bf16_f32 v131, v132, v133
	ds_write_b64 v211, v[130:131]
	v_mfma_f32_32x32x16_bf16 v[18:33], v[122:125], v[178:181], v[18:33]
	s_nop 1
	v_exp_f32_e32 v131, v4
	v_exp_f32_e32 v130, v8
	v_exp_f32_e32 v133, v12
	v_exp_f32_e32 v132, v16
	v_mfma_f32_32x32x16_bf16 v[18:33], v[118:121], v[170:173], v[18:33]
	v_exp_f32_e32 v2, v2
	v_exp_f32_e32 v6, v6
	v_exp_f32_e32 v10, v10
	v_exp_f32_e32 v12, v14
	v_add_f32_e32 v4, 1.0, v131
	v_add_f32_e32 v8, 1.0, v130
	v_add_f32_e32 v14, 1.0, v133
	v_add_f32_e32 v16, 1.0, v132
	v_mfma_f32_32x32x16_bf16 v[18:33], v[114:117], v[166:169], v[18:33]
	v_exp_f32_e32 v3, v3
	v_fmac_f32_e32 v4, v2, v4
	v_exp_f32_e32 v2, v7
	v_fmac_f32_e32 v8, v6, v8
	v_exp_f32_e32 v6, v11
	v_exp_f32_e32 v7, v15
	v_fmac_f32_e32 v14, v10, v14
	v_fmac_f32_e32 v16, v12, v16
	v_mfma_f32_32x32x16_bf16 v[18:33], v[110:113], v[162:165], v[18:33]
	v_add_f32_e32 v10, 1.0, v3
	v_rcp_f32_e32 v3, v4
	v_add_f32_e32 v4, 1.0, v2
	v_rcp_f32_e32 v2, v8
	v_rcp_f32_e32 v135, v14
	v_rcp_f32_e32 v134, v16
	v_mfma_f32_32x32x16_bf16 v[18:33], v[106:109], v[174:177], v[18:33]
	v_add_f32_e32 v6, 1.0, v6
	v_add_f32_e32 v7, 1.0, v7
	v_rcp_f32_e32 v137, v10
	v_rcp_f32_e32 v136, v4
	v_exp_f32_e32 v140, v5
	v_exp_f32_e32 v141, v9
	v_mfma_f32_32x32x16_bf16 v[18:33], v[102:105], v[182:185], v[18:33]
	v_rcp_f32_e32 v139, v6
	v_rcp_f32_e32 v138, v7
	v_exp_f32_e32 v146, v13
	v_exp_f32_e32 v147, v17
	v_pk_fma_f32 v[4:5], v[130:131], s[12:13], v[218:219] op_sel_hi:[1,0,0]
	v_mfma_f32_32x32x16_bf16 v[18:33], v[98:101], v[142:145], v[18:33]
	v_mul_f32_e64 v130, v4, v2
	v_mul_f32_e64 v131, v5, v3
	ds_read_b128 v[2:5], v231 offset:37056
	ds_read_b128 v[6:9], v231 offset:37072
	ds_read_b128 v[10:13], v231 offset:37088
	ds_read_b128 v[14:17], v231 offset:37104
	v_pk_fma_f32 v[224:225], v[136:137], v[204:205], v[130:131]
	v_pk_fma_f32 v[130:131], v[132:133], s[12:13], v[218:219] op_sel_hi:[1,0,0]
	s_nop 0
	v_pk_mul_f32 v[130:131], v[130:131], v[134:135]
	s_nop 0
	v_pk_fma_f32 v[226:227], v[138:139], v[202:203], v[130:131]
	s_waitcnt lgkmcnt(8)
	v_mfma_f32_32x32x16_bf16 v[18:33], v[94:97], v[154:157], v[18:33]
	v_add_f32_e32 v130, 1.0, v140
	v_exp_f32_e32 v131, v225
	v_add_f32_e32 v132, 1.0, v141
	v_exp_f32_e32 v133, v224
	v_exp_f32_e32 v134, v227
	v_exp_f32_e32 v135, v226
	v_add_f32_e32 v136, 1.0, v146
	v_add_f32_e32 v137, 1.0, v147
	s_waitcnt lgkmcnt(7)
	v_mfma_f32_32x32x16_bf16 v[18:33], v[90:93], v[158:161], v[18:33]
	v_fmac_f32_e32 v130, v130, v131
	v_fmac_f32_e32 v132, v132, v133
	v_fmac_f32_e32 v136, v136, v134
	v_fmac_f32_e32 v137, v137, v135
	s_waitcnt lgkmcnt(6)
	v_mfma_f32_32x32x16_bf16 v[18:33], v[86:89], v[186:189], v[18:33]
	v_rcp_f32_e32 v130, v130
	v_rcp_f32_e32 v132, v132
	v_rcp_f32_e32 v136, v136
	v_rcp_f32_e32 v137, v137
	s_waitcnt lgkmcnt(5)
	v_mfma_f32_32x32x16_bf16 v[18:33], v[82:85], v[190:193], v[18:33]
	v_fma_f32 v130, -v131, v130, v130
	v_fma_f32 v131, -v133, v132, v132
	v_fma_f32 v132, -v134, v136, v136
	v_fma_f32 v133, -v135, v137, v137
	v_cvt_pk_bf16_f32 v130, v130, v131
	v_cvt_pk_bf16_f32 v131, v132, v133
	ds_write_b64 v211, v[130:131] offset:8
	s_waitcnt lgkmcnt(0)
	s_barrier
	v_mfma_f32_32x32x16_bf16 v[2:17], v[78:81], v[194:197], v[2:17]
	ds_read_b32 v233, v232 offset:128
	ds_read_b128 v[202:205], v210
	v_add_u32_e32 v216, v230, v216
	v_mfma_f32_32x32x16_bf16 v[2:17], v[74:77], v[178:181], v[2:17]
	ds_read_b128 v[194:197], v210 offset:1024
	v_exp_f32_e32 v147, v20
	v_exp_f32_e32 v146, v24
	v_exp_f32_e32 v149, v28
	v_exp_f32_e32 v148, v32
	v_mfma_f32_32x32x16_bf16 v[2:17], v[70:73], v[170:173], v[2:17]
	ds_read_b128 v[138:141], v210 offset:2048
	v_exp_f32_e32 v18, v18
	v_exp_f32_e32 v22, v22
	v_exp_f32_e32 v24, v26
	v_exp_f32_e32 v26, v30
	v_add_f32_e32 v20, 1.0, v147
	v_add_f32_e32 v28, 1.0, v146
	v_add_f32_e32 v30, 1.0, v149
	v_add_f32_e32 v32, 1.0, v148
	v_mfma_f32_32x32x16_bf16 v[2:17], v[66:69], v[166:169], v[2:17]
	ds_read_b128 v[134:137], v210 offset:3072
	v_exp_f32_e32 v19, v19
	v_exp_f32_e32 v23, v23
	v_exp_f32_e32 v27, v27
	v_exp_f32_e32 v31, v31
	v_fmac_f32_e32 v20, v18, v20
	v_fmac_f32_e32 v28, v22, v28
	v_fmac_f32_e32 v30, v24, v30
	v_fmac_f32_e32 v32, v26, v32
	v_mfma_f32_32x32x16_bf16 v[2:17], v[62:65], v[162:165], v[2:17]
	ds_read_b128 v[166:169], v210 offset:4096
	v_add_f32_e32 v22, 1.0, v19
	v_rcp_f32_e32 v19, v20
	v_rcp_f32_e32 v18, v28
	v_rcp_f32_e32 v151, v30
	v_rcp_f32_e32 v150, v32
	v_add_f32_e32 v20, 1.0, v23
	v_mfma_f32_32x32x16_bf16 v[2:17], v[58:61], v[174:177], v[2:17]
	ds_read_b128 v[162:165], v210 offset:5120
	v_rcp_f32_e32 v153, v22
	v_rcp_f32_e32 v152, v20
	v_add_f32_e32 v23, 1.0, v27
	v_add_f32_e32 v20, 1.0, v31
	v_exp_f32_e32 v180, v21
	v_exp_f32_e32 v181, v25
	v_mfma_f32_32x32x16_bf16 v[2:17], v[54:57], v[182:185], v[2:17]
	ds_read_b128 v[170:173], v210 offset:6144
	v_rcp_f32_e32 v175, v23
	v_rcp_f32_e32 v174, v20
	v_exp_f32_e32 v176, v29
	v_exp_f32_e32 v177, v33
	v_mfma_f32_32x32x16_bf16 v[2:17], v[50:53], v[142:145], v[2:17]
	v_mov_b64_e32 v[178:179], s[0:1]
	v_fma_f32 v20, v146, s12, v178
	v_fma_f32 v21, v147, s12, v178
	ds_read_b128 v[130:133], v210 offset:7168
	v_mul_f32_e64 v146, v20, v18
	v_mul_f32_e64 v147, v21, v19
	ds_read_b128 v[18:21], v231 offset:36928
	ds_read_b128 v[22:25], v231 offset:36944
	ds_read_b128 v[26:29], v231 offset:36960
	ds_read_b128 v[30:33], v231 offset:36976
	v_pk_fma_f32 v[142:143], v[148:149], s[12:13], v[178:179] op_sel_hi:[1,0,0]
	v_pk_fma_f32 v[220:221], v[152:153], v[200:201], v[146:147]
	v_pk_mul_f32 v[142:143], v[142:143], v[150:151]
	s_nop 0
	v_pk_fma_f32 v[222:223], v[174:175], v[198:199], v[142:143]
	v_mfma_f32_32x32x16_bf16 v[2:17], v[46:49], v[154:157], v[2:17]
	ds_read_b128 v[146:149], v216 offset:16384
	v_add_f32_e32 v142, 1.0, v180
	v_exp_f32_e32 v143, v221
	v_exp_f32_e32 v144, v220
	v_exp_f32_e32 v145, v223
	v_exp_f32_e32 v180, v222
	v_add_f32_e32 v154, 1.0, v181
	v_add_f32_e32 v155, 1.0, v176
	v_add_f32_e32 v156, 1.0, v177
	v_mfma_f32_32x32x16_bf16 v[2:17], v[42:45], v[158:161], v[2:17]
	ds_read_b128 v[150:153], v216 offset:16416
	v_fmac_f32_e32 v142, v142, v143
	v_fmac_f32_e32 v154, v154, v144
	v_fmac_f32_e32 v155, v155, v145
	v_fmac_f32_e32 v156, v156, v180
	v_mfma_f32_32x32x16_bf16 v[2:17], v[38:41], v[186:189], v[2:17]
	ds_read_b128 v[174:177], v216 offset:16448
	v_rcp_f32_e32 v142, v142
	v_rcp_f32_e32 v154, v154
	v_rcp_f32_e32 v155, v155
	v_rcp_f32_e32 v156, v156
	v_mfma_f32_32x32x16_bf16 v[2:17], v[34:37], v[190:193], v[2:17]
	ds_read_b128 v[198:201], v216 offset:16480
	v_fma_f32 v142, -v143, v142, v142
	v_fma_f32 v143, -v144, v154, v154
	v_fma_f32 v144, -v145, v155, v155
	v_fma_f32 v145, -v180, v156, v156
	s_waitcnt lgkmcnt(4)
	v_mfma_f32_32x32x16_bf16 v[18:33], v[126:129], v[202:205], v[18:33]
	v_cvt_pk_bf16_f32 v142, v142, v143
	v_cvt_pk_bf16_f32 v143, v144, v145
	ds_write_b64 v211, v[142:143] offset:8192
	v_mfma_f32_32x32x16_bf16 v[18:33], v[122:125], v[194:197], v[18:33]
	s_nop 1
	v_exp_f32_e32 v143, v4
	v_exp_f32_e32 v142, v8
	v_exp_f32_e32 v145, v12
	v_exp_f32_e32 v144, v16
	v_mfma_f32_32x32x16_bf16 v[18:33], v[118:121], v[138:141], v[18:33]
	v_exp_f32_e32 v2, v2
	v_exp_f32_e32 v6, v6
	v_exp_f32_e32 v10, v10
	v_exp_f32_e32 v12, v14
	v_add_f32_e32 v4, 1.0, v143
	v_add_f32_e32 v8, 1.0, v142
	v_add_f32_e32 v14, 1.0, v145
	v_add_f32_e32 v16, 1.0, v144
	v_mfma_f32_32x32x16_bf16 v[18:33], v[114:117], v[134:137], v[18:33]
	v_exp_f32_e32 v3, v3
	v_fmac_f32_e32 v4, v2, v4
	v_exp_f32_e32 v2, v7
	v_fmac_f32_e32 v8, v6, v8
	v_exp_f32_e32 v6, v11
	v_exp_f32_e32 v7, v15
	v_fmac_f32_e32 v14, v10, v14
	v_fmac_f32_e32 v16, v12, v16
	v_mfma_f32_32x32x16_bf16 v[18:33], v[110:113], v[166:169], v[18:33]
	v_add_f32_e32 v10, 1.0, v3
	v_rcp_f32_e32 v3, v4
	v_add_f32_e32 v4, 1.0, v2
	v_rcp_f32_e32 v2, v8
	v_rcp_f32_e32 v155, v14
	v_rcp_f32_e32 v154, v16
	v_mfma_f32_32x32x16_bf16 v[18:33], v[106:109], v[162:165], v[18:33]
	v_add_f32_e32 v6, 1.0, v6
	v_add_f32_e32 v7, 1.0, v7
	v_rcp_f32_e32 v157, v10
	v_rcp_f32_e32 v156, v4
	v_exp_f32_e32 v160, v5
	v_exp_f32_e32 v161, v9
	v_mfma_f32_32x32x16_bf16 v[18:33], v[102:105], v[170:173], v[18:33]
	v_rcp_f32_e32 v159, v6
	v_rcp_f32_e32 v158, v7
	v_exp_f32_e32 v180, v13
	v_exp_f32_e32 v181, v17
	v_pk_fma_f32 v[4:5], v[142:143], s[12:13], v[178:179] op_sel_hi:[1,0,0]
	v_mfma_f32_32x32x16_bf16 v[18:33], v[98:101], v[130:133], v[18:33]
	v_mul_f32_e64 v142, v4, v2
	v_mul_f32_e64 v143, v5, v3
	ds_read_b128 v[2:5], v231 offset:37056
	ds_read_b128 v[6:9], v231 offset:37072
	ds_read_b128 v[10:13], v231 offset:37088
	ds_read_b128 v[14:17], v231 offset:37104
	v_pk_fma_f32 v[216:217], v[156:157], v[206:207], v[142:143]
	v_pk_fma_f32 v[142:143], v[144:145], s[12:13], v[178:179] op_sel_hi:[1,0,0]
	s_nop 0
	v_pk_mul_f32 v[142:143], v[142:143], v[154:155]
	s_nop 0
	v_pk_fma_f32 v[218:219], v[158:159], v[208:209], v[142:143]
	s_waitcnt lgkmcnt(8)
	v_mfma_f32_32x32x16_bf16 v[18:33], v[94:97], v[146:149], v[18:33]
	v_add_f32_e32 v142, 1.0, v160
	v_exp_f32_e32 v143, v217
	v_add_f32_e32 v144, 1.0, v161
	v_exp_f32_e32 v145, v216
	v_exp_f32_e32 v154, v219
	v_exp_f32_e32 v155, v218
	v_add_f32_e32 v156, 1.0, v180
	v_add_f32_e32 v157, 1.0, v181
	s_waitcnt lgkmcnt(7)
	v_mfma_f32_32x32x16_bf16 v[18:33], v[90:93], v[150:153], v[18:33]
	v_fmac_f32_e32 v142, v142, v143
	v_fmac_f32_e32 v144, v144, v145
	v_fmac_f32_e32 v156, v156, v154
	v_fmac_f32_e32 v157, v157, v155
	s_waitcnt lgkmcnt(6)
	v_mfma_f32_32x32x16_bf16 v[18:33], v[86:89], v[174:177], v[18:33]
	v_rcp_f32_e32 v142, v142
	v_rcp_f32_e32 v144, v144
	v_rcp_f32_e32 v156, v156
	v_rcp_f32_e32 v157, v157
	s_waitcnt lgkmcnt(5)
	v_mfma_f32_32x32x16_bf16 v[18:33], v[82:85], v[198:201], v[18:33]
	v_fma_f32 v142, -v143, v142, v142
	v_fma_f32 v143, -v145, v144, v144
	v_fma_f32 v144, -v154, v156, v156
	v_fma_f32 v145, -v155, v157, v157
	v_cvt_pk_bf16_f32 v142, v142, v143
	v_cvt_pk_bf16_f32 v143, v144, v145
	ds_write_b64 v211, v[142:143] offset:8200
	s_waitcnt lgkmcnt(0)
	s_barrier
	v_mfma_f32_32x32x16_bf16 v[2:17], v[78:81], v[202:205], v[2:17]
	v_add_u32_e32 v234, v230, v233
	ds_read_b32 v233, v232 offset:256
	ds_read_b128 v[206:209], v210 offset:8192
	v_mfma_f32_32x32x16_bf16 v[2:17], v[74:77], v[194:197], v[2:17]
	ds_read_b128 v[190:193], v210 offset:9216
	v_exp_f32_e32 v179, v20
	v_exp_f32_e32 v178, v24
	v_exp_f32_e32 v181, v28
	v_exp_f32_e32 v180, v32
	v_mfma_f32_32x32x16_bf16 v[2:17], v[70:73], v[138:141], v[2:17]
	ds_read_b128 v[158:161], v210 offset:10240
	v_exp_f32_e32 v18, v18
	v_exp_f32_e32 v22, v22
	v_exp_f32_e32 v24, v26
	v_exp_f32_e32 v26, v30
	v_add_f32_e32 v20, 1.0, v179
	v_add_f32_e32 v28, 1.0, v178
	v_add_f32_e32 v30, 1.0, v181
	v_add_f32_e32 v32, 1.0, v180
	v_mfma_f32_32x32x16_bf16 v[2:17], v[66:69], v[134:137], v[2:17]
	ds_read_b128 v[142:145], v210 offset:11264
	v_exp_f32_e32 v19, v19
	v_exp_f32_e32 v23, v23
	v_exp_f32_e32 v27, v27
	v_exp_f32_e32 v31, v31
	v_fmac_f32_e32 v20, v18, v20
	v_fmac_f32_e32 v28, v22, v28
	v_fmac_f32_e32 v30, v24, v30
	v_fmac_f32_e32 v32, v26, v32
	v_mfma_f32_32x32x16_bf16 v[2:17], v[62:65], v[166:169], v[2:17]
	ds_read_b128 v[154:157], v210 offset:12288
	v_add_f32_e32 v22, 1.0, v19
	v_rcp_f32_e32 v19, v20
	v_rcp_f32_e32 v18, v28
	v_rcp_f32_e32 v139, v30
	v_rcp_f32_e32 v138, v32
	v_add_f32_e32 v20, 1.0, v23
	v_mfma_f32_32x32x16_bf16 v[2:17], v[58:61], v[162:165], v[2:17]
	ds_read_b128 v[182:185], v210 offset:13312
	v_rcp_f32_e32 v141, v22
	v_rcp_f32_e32 v140, v20
	v_add_f32_e32 v23, 1.0, v27
	v_add_f32_e32 v20, 1.0, v31
	v_exp_f32_e32 v168, v21
	v_exp_f32_e32 v169, v25
	v_mfma_f32_32x32x16_bf16 v[2:17], v[54:57], v[170:173], v[2:17]
	ds_read_b128 v[186:189], v210 offset:14336
	v_rcp_f32_e32 v163, v23
	v_rcp_f32_e32 v162, v20
	v_exp_f32_e32 v194, v29
	v_exp_f32_e32 v195, v33
	v_mfma_f32_32x32x16_bf16 v[2:17], v[50:53], v[130:133], v[2:17]
	v_mov_b64_e32 v[164:165], s[0:1]
	v_fma_f32 v20, v178, s12, v164
	v_fma_f32 v21, v179, s12, v164
	ds_read_b128 v[134:137], v210 offset:15360
	v_mul_f32_e64 v166, v20, v18
	v_mul_f32_e64 v167, v21, v19
	ds_read_b128 v[18:21], v231 offset:36928
	ds_read_b128 v[22:25], v231 offset:36944
	ds_read_b128 v[26:29], v231 offset:36960
	ds_read_b128 v[30:33], v231 offset:36976
	v_pk_fma_f32 v[130:131], v[180:181], s[12:13], v[164:165] op_sel_hi:[1,0,0]
	v_pk_fma_f32 v[214:215], v[140:141], v[214:215], v[166:167]
	v_pk_mul_f32 v[130:131], v[130:131], v[138:139]
	s_nop 0
	v_pk_fma_f32 v[212:213], v[162:163], v[212:213], v[130:131]
	v_mfma_f32_32x32x16_bf16 v[2:17], v[46:49], v[146:149], v[2:17]
	ds_read_b128 v[138:141], v234 offset:16384
	v_add_f32_e32 v130, 1.0, v168
	v_exp_f32_e32 v131, v215
	v_exp_f32_e32 v132, v214
	v_exp_f32_e32 v133, v213
	v_exp_f32_e32 v162, v212
	v_add_f32_e32 v163, 1.0, v169
	v_add_f32_e32 v166, 1.0, v194
	v_add_f32_e32 v167, 1.0, v195
	v_mfma_f32_32x32x16_bf16 v[2:17], v[42:45], v[150:153], v[2:17]
	ds_read_b128 v[146:149], v234 offset:16416
	v_fmac_f32_e32 v130, v130, v131
	v_fmac_f32_e32 v163, v163, v132
	v_fmac_f32_e32 v166, v166, v133
	v_fmac_f32_e32 v167, v167, v162
	v_mfma_f32_32x32x16_bf16 v[2:17], v[38:41], v[174:177], v[2:17]
	ds_read_b128 v[150:153], v234 offset:16448
	v_rcp_f32_e32 v130, v130
	v_rcp_f32_e32 v163, v163
	v_rcp_f32_e32 v166, v166
	v_rcp_f32_e32 v167, v167
	v_mfma_f32_32x32x16_bf16 v[2:17], v[34:37], v[198:201], v[2:17]
	ds_read_b128 v[178:181], v234 offset:16480
	v_fma_f32 v130, -v131, v130, v130
	v_fma_f32 v131, -v132, v163, v163
	v_fma_f32 v132, -v133, v166, v166
	v_fma_f32 v133, -v162, v167, v167
	s_waitcnt lgkmcnt(4)
	v_mfma_f32_32x32x16_bf16 v[18:33], v[126:129], v[206:209], v[18:33]
	v_cvt_pk_bf16_f32 v130, v130, v131
	v_cvt_pk_bf16_f32 v131, v132, v133
	ds_write_b64 v211, v[130:131]
	v_mfma_f32_32x32x16_bf16 v[18:33], v[122:125], v[190:193], v[18:33]
	s_nop 1
	v_exp_f32_e32 v131, v4
	v_exp_f32_e32 v130, v8
	v_exp_f32_e32 v133, v12
	v_exp_f32_e32 v132, v16
	v_mfma_f32_32x32x16_bf16 v[18:33], v[118:121], v[158:161], v[18:33]
	v_exp_f32_e32 v2, v2
	v_exp_f32_e32 v6, v6
	v_exp_f32_e32 v10, v10
	v_exp_f32_e32 v12, v14
	v_add_f32_e32 v4, 1.0, v131
	v_add_f32_e32 v8, 1.0, v130
	v_add_f32_e32 v14, 1.0, v133
	v_add_f32_e32 v16, 1.0, v132
	v_mfma_f32_32x32x16_bf16 v[18:33], v[114:117], v[142:145], v[18:33]
	v_exp_f32_e32 v3, v3
	v_fmac_f32_e32 v4, v2, v4
	v_exp_f32_e32 v2, v7
	v_fmac_f32_e32 v8, v6, v8
	v_exp_f32_e32 v6, v11
	v_exp_f32_e32 v7, v15
	v_fmac_f32_e32 v14, v10, v14
	v_fmac_f32_e32 v16, v12, v16
	v_mfma_f32_32x32x16_bf16 v[18:33], v[110:113], v[154:157], v[18:33]
	v_add_f32_e32 v10, 1.0, v3
	v_rcp_f32_e32 v3, v4
	v_add_f32_e32 v4, 1.0, v2
	v_rcp_f32_e32 v2, v8
	v_rcp_f32_e32 v163, v14
	v_rcp_f32_e32 v162, v16
	v_mfma_f32_32x32x16_bf16 v[18:33], v[106:109], v[182:185], v[18:33]
	v_add_f32_e32 v6, 1.0, v6
	v_add_f32_e32 v7, 1.0, v7
	v_rcp_f32_e32 v167, v10
	v_rcp_f32_e32 v166, v4
	v_exp_f32_e32 v170, v5
	v_exp_f32_e32 v171, v9
	v_mfma_f32_32x32x16_bf16 v[18:33], v[102:105], v[186:189], v[18:33]
	v_rcp_f32_e32 v169, v6
	v_rcp_f32_e32 v168, v7
	v_exp_f32_e32 v172, v13
	v_exp_f32_e32 v173, v17
	v_pk_fma_f32 v[4:5], v[130:131], s[12:13], v[164:165] op_sel_hi:[1,0,0]
	v_mfma_f32_32x32x16_bf16 v[18:33], v[98:101], v[134:137], v[18:33]
	v_mul_f32_e64 v130, v4, v2
	v_mul_f32_e64 v131, v5, v3
	ds_read_b128 v[2:5], v231 offset:37056
	ds_read_b128 v[6:9], v231 offset:37072
	ds_read_b128 v[10:13], v231 offset:37088
	ds_read_b128 v[14:17], v231 offset:37104
	v_pk_fma_f32 v[204:205], v[166:167], v[224:225], v[130:131]
	v_pk_fma_f32 v[130:131], v[132:133], s[12:13], v[164:165] op_sel_hi:[1,0,0]
	s_nop 0
	v_pk_mul_f32 v[130:131], v[130:131], v[162:163]
	s_nop 0
	v_pk_fma_f32 v[202:203], v[168:169], v[226:227], v[130:131]
	s_waitcnt lgkmcnt(8)
	v_mfma_f32_32x32x16_bf16 v[18:33], v[94:97], v[138:141], v[18:33]
	v_add_f32_e32 v130, 1.0, v170
	v_exp_f32_e32 v131, v205
	v_add_f32_e32 v132, 1.0, v171
	v_exp_f32_e32 v133, v204
	v_exp_f32_e32 v162, v203
	v_exp_f32_e32 v163, v202
	v_add_f32_e32 v164, 1.0, v172
	v_add_f32_e32 v165, 1.0, v173
	s_waitcnt lgkmcnt(7)
	v_mfma_f32_32x32x16_bf16 v[18:33], v[90:93], v[146:149], v[18:33]
	v_fmac_f32_e32 v130, v130, v131
	v_fmac_f32_e32 v132, v132, v133
	v_fmac_f32_e32 v164, v164, v162
	v_fmac_f32_e32 v165, v165, v163
	s_waitcnt lgkmcnt(6)
	v_mfma_f32_32x32x16_bf16 v[18:33], v[86:89], v[150:153], v[18:33]
	v_rcp_f32_e32 v130, v130
	v_rcp_f32_e32 v132, v132
	v_rcp_f32_e32 v164, v164
	v_rcp_f32_e32 v165, v165
	s_waitcnt lgkmcnt(5)
	v_mfma_f32_32x32x16_bf16 v[18:33], v[82:85], v[178:181], v[18:33]
	v_fma_f32 v130, -v131, v130, v130
	v_fma_f32 v131, -v133, v132, v132
	v_fma_f32 v132, -v162, v164, v164
	v_fma_f32 v133, -v163, v165, v165
	v_cvt_pk_bf16_f32 v130, v130, v131
	v_cvt_pk_bf16_f32 v131, v132, v133
	ds_write_b64 v211, v[130:131] offset:8
	s_waitcnt lgkmcnt(0)
	s_barrier
	s_branch .LBB1_13
.LBB1_30:
	v_mfma_f32_32x32x16_bf16 v[2:17], v[78:81], v[174:177], v[2:17]
	ds_read_b128 v[178:181], v210 offset:8192
	v_add_u32_e32 v182, v230, v194
	v_mfma_f32_32x32x16_bf16 v[2:17], v[74:77], v[170:173], v[2:17]
	ds_read_b128 v[174:177], v210 offset:9216
	v_exp_f32_e32 v20, v20
	v_exp_f32_e32 v24, v24
	v_exp_f32_e32 v28, v28
	v_exp_f32_e32 v32, v32
	v_mfma_f32_32x32x16_bf16 v[2:17], v[70:73], v[166:169], v[2:17]
	ds_read_b128 v[170:173], v210 offset:10240
	v_exp_f32_e32 v18, v18
	v_exp_f32_e32 v22, v22
	v_exp_f32_e32 v26, v26
	v_exp_f32_e32 v30, v30
	v_add_f32_e32 v183, 1.0, v20
	v_add_f32_e32 v184, 1.0, v24
	v_add_f32_e32 v185, 1.0, v28
	v_add_f32_e32 v186, 1.0, v32
	v_mfma_f32_32x32x16_bf16 v[2:17], v[66:69], v[162:165], v[2:17]
	ds_read_b128 v[166:169], v210 offset:11264
	v_exp_f32_e32 v19, v19
	v_fmac_f32_e32 v183, v18, v183
	v_exp_f32_e32 v18, v23
	v_exp_f32_e32 v23, v27
	v_exp_f32_e32 v27, v31
	v_fmac_f32_e32 v184, v22, v184
	v_fmac_f32_e32 v185, v26, v185
	v_fmac_f32_e32 v186, v30, v186
	v_mfma_f32_32x32x16_bf16 v[2:17], v[62:65], v[158:161], v[2:17]
	ds_read_b128 v[162:165], v210 offset:12288
	v_rcp_f32_e32 v22, v183
	v_rcp_f32_e32 v26, v184
	v_rcp_f32_e32 v30, v185
	v_rcp_f32_e32 v31, v186
	v_mov_b32_e32 v183, 0xc038aa3b
	v_add_f32_e32 v19, 1.0, v19
	v_fmamk_f32 v20, v20, 0x4038aa3b, v183
	v_add_f32_e32 v18, 1.0, v18
	v_fmamk_f32 v24, v24, 0x4038aa3b, v183
	v_mfma_f32_32x32x16_bf16 v[2:17], v[58:61], v[154:157], v[2:17]
	ds_read_b128 v[158:161], v210 offset:13312
	v_rcp_f32_e32 v19, v19
	v_add_f32_e32 v23, 1.0, v23
	v_rcp_f32_e32 v184, v18
	v_exp_f32_e32 v185, v21
	v_exp_f32_e32 v186, v25
	v_fmamk_f32 v18, v28, 0x4038aa3b, v183
	v_add_f32_e32 v21, 1.0, v27
	v_fmamk_f32 v25, v32, 0x4038aa3b, v183
	v_mfma_f32_32x32x16_bf16 v[2:17], v[54:57], v[142:145], v[2:17]
	ds_read_b128 v[154:157], v210 offset:14336
	v_mul_f32_e32 v187, v20, v22
	v_rcp_f32_e32 v188, v23
	v_rcp_f32_e32 v189, v21
	v_exp_f32_e32 v190, v29
	v_exp_f32_e32 v191, v33
	v_mul_f32_e32 v192, v24, v26
	v_mul_f32_e32 v193, v18, v30
	v_mul_f32_e32 v194, v25, v31
	v_mfma_f32_32x32x16_bf16 v[2:17], v[50:53], v[130:133], v[2:17]
	ds_read_b128 v[142:145], v210 offset:15360
	v_fmac_f32_e32 v187, v19, v215
	ds_read_b128 v[18:21], v231 offset:36928
	ds_read_b128 v[22:25], v231 offset:36944
	ds_read_b128 v[26:29], v231 offset:36960
	ds_read_b128 v[30:33], v231 offset:36976
	v_fmac_f32_e32 v192, v184, v214
	v_fmac_f32_e32 v193, v188, v213
	v_fmac_f32_e32 v194, v189, v212
	v_mfma_f32_32x32x16_bf16 v[2:17], v[46:49], v[134:137], v[2:17]
	ds_read_b128 v[130:133], v182 offset:16384
	v_add_f32_e32 v184, 1.0, v185
	v_exp_f32_e32 v185, v187
	v_exp_f32_e32 v187, v192
	v_exp_f32_e32 v188, v193
	v_exp_f32_e32 v189, v194
	v_add_f32_e32 v186, 1.0, v186
	v_add_f32_e32 v190, 1.0, v190
	v_add_f32_e32 v191, 1.0, v191
	v_mfma_f32_32x32x16_bf16 v[2:17], v[42:45], v[138:141], v[2:17]
	ds_read_b128 v[134:137], v182 offset:16416
	v_fmac_f32_e32 v184, v184, v185
	v_fmac_f32_e32 v186, v186, v187
	v_fmac_f32_e32 v190, v190, v188
	v_fmac_f32_e32 v191, v191, v189
	v_mfma_f32_32x32x16_bf16 v[2:17], v[38:41], v[146:149], v[2:17]
	ds_read_b128 v[138:141], v182 offset:16448
	v_rcp_f32_e32 v184, v184
	v_rcp_f32_e32 v186, v186
	v_rcp_f32_e32 v190, v190
	v_rcp_f32_e32 v191, v191
	v_mfma_f32_32x32x16_bf16 v[2:17], v[34:37], v[150:153], v[2:17]
	ds_read_b128 v[146:149], v182 offset:16480
	v_fma_f32 v182, -v185, v184, v184
	v_fma_f32 v184, -v187, v186, v186
	v_fma_f32 v185, -v188, v190, v190
	v_fma_f32 v186, -v189, v191, v191
	s_waitcnt lgkmcnt(4)
	v_mfma_f32_32x32x16_bf16 v[18:33], v[126:129], v[178:181], v[18:33]
	v_cvt_pk_bf16_f32 v150, v182, v184
	v_cvt_pk_bf16_f32 v151, v185, v186
	ds_write_b64 v211, v[150:151]
	v_mfma_f32_32x32x16_bf16 v[18:33], v[122:125], v[174:177], v[18:33]
	s_nop 1
	v_exp_f32_e32 v4, v4
	v_exp_f32_e32 v8, v8
	v_exp_f32_e32 v12, v12
	v_exp_f32_e32 v16, v16
	v_mfma_f32_32x32x16_bf16 v[18:33], v[118:121], v[170:173], v[18:33]
	v_exp_f32_e32 v2, v2
	v_exp_f32_e32 v6, v6
	v_exp_f32_e32 v10, v10
	v_exp_f32_e32 v14, v14
	v_add_f32_e32 v122, 1.0, v4
	v_add_f32_e32 v123, 1.0, v8
	v_add_f32_e32 v118, 1.0, v12
	v_add_f32_e32 v119, 1.0, v16
	v_mfma_f32_32x32x16_bf16 v[18:33], v[114:117], v[166:169], v[18:33]
	v_exp_f32_e32 v3, v3
	v_fmac_f32_e32 v122, v2, v122
	v_exp_f32_e32 v2, v7
	v_fmac_f32_e32 v123, v6, v123
	v_exp_f32_e32 v6, v11
	v_exp_f32_e32 v7, v15
	v_fmac_f32_e32 v118, v10, v118
	v_fmac_f32_e32 v119, v14, v119
	v_mfma_f32_32x32x16_bf16 v[18:33], v[110:113], v[162:165], v[18:33]
	v_rcp_f32_e32 v10, v122
	v_rcp_f32_e32 v11, v123
	v_rcp_f32_e32 v14, v118
	v_rcp_f32_e32 v15, v119
	v_add_f32_e32 v3, 1.0, v3
	v_fmamk_f32 v4, v4, 0x4038aa3b, v183
	v_add_f32_e32 v2, 1.0, v2
	v_fmamk_f32 v8, v8, 0x4038aa3b, v183
	v_mfma_f32_32x32x16_bf16 v[18:33], v[106:109], v[158:161], v[18:33]
	v_rcp_f32_e32 v3, v3
	v_rcp_f32_e32 v2, v2
	v_add_f32_e32 v6, 1.0, v6
	v_fmamk_f32 v12, v12, 0x4038aa3b, v183
	v_exp_f32_e32 v110, v5
	v_add_f32_e32 v5, 1.0, v7
	v_exp_f32_e32 v111, v9
	v_fmac_f32_e32 v183, 0x4038aa3b, v16
	v_mfma_f32_32x32x16_bf16 v[18:33], v[102:105], v[154:157], v[18:33]
	v_mul_f32_e32 v106, v4, v10
	v_mul_f32_e32 v107, v8, v11
	v_rcp_f32_e32 v108, v6
	v_rcp_f32_e32 v109, v5
	v_exp_f32_e32 v112, v13
	v_exp_f32_e32 v113, v17
	v_mul_f32_e32 v102, v12, v14
	v_mul_f32_e32 v103, v183, v15
	v_mfma_f32_32x32x16_bf16 v[18:33], v[98:101], v[142:145], v[18:33]
	v_fmac_f32_e32 v106, v3, v205
	v_fmac_f32_e32 v107, v2, v204
	ds_read_b128 v[2:5], v231 offset:37056
	ds_read_b128 v[6:9], v231 offset:37072
	ds_read_b128 v[10:13], v231 offset:37088
	ds_read_b128 v[14:17], v231 offset:37104
	v_fmac_f32_e32 v102, v108, v203
	v_fmac_f32_e32 v103, v109, v202
	s_waitcnt lgkmcnt(8)
	v_mfma_f32_32x32x16_bf16 v[18:33], v[94:97], v[130:133], v[18:33]
	v_add_f32_e32 v98, 1.0, v110
	v_exp_f32_e32 v99, v106
	v_add_f32_e32 v100, 1.0, v111
	v_exp_f32_e32 v101, v107
	v_exp_f32_e32 v102, v102
	v_exp_f32_e32 v103, v103
	v_add_f32_e32 v94, 1.0, v112
	v_add_f32_e32 v95, 1.0, v113
	s_waitcnt lgkmcnt(7)
	v_mfma_f32_32x32x16_bf16 v[18:33], v[90:93], v[134:137], v[18:33]
	v_fmac_f32_e32 v98, v98, v99
	v_fmac_f32_e32 v100, v100, v101
	v_fmac_f32_e32 v94, v94, v102
	v_fmac_f32_e32 v95, v95, v103
	s_waitcnt lgkmcnt(6)
	v_mfma_f32_32x32x16_bf16 v[18:33], v[86:89], v[138:141], v[18:33]
	v_rcp_f32_e32 v90, v98
	v_rcp_f32_e32 v91, v100
	v_rcp_f32_e32 v92, v94
	v_rcp_f32_e32 v93, v95
	s_waitcnt lgkmcnt(5)
	v_mfma_f32_32x32x16_bf16 v[18:33], v[82:85], v[146:149], v[18:33]
	v_fma_f32 v86, -v99, v90, v90
	v_fma_f32 v87, -v101, v91, v91
	v_fma_f32 v88, -v102, v92, v92
	v_fma_f32 v89, -v103, v93, v93
	v_cvt_pk_bf16_f32 v82, v86, v87
	v_cvt_pk_bf16_f32 v83, v88, v89
	ds_write_b64 v211, v[82:83] offset:8
	s_waitcnt lgkmcnt(0)
	s_barrier
	v_mfma_f32_32x32x16_bf16 v[2:17], v[78:81], v[178:181], v[2:17]
	v_exp_f32_e32 v20, v20
	v_exp_f32_e32 v24, v24
	v_exp_f32_e32 v28, v28
	v_exp_f32_e32 v32, v32
	v_mfma_f32_32x32x16_bf16 v[2:17], v[74:77], v[174:177], v[2:17]
	v_exp_f32_e32 v18, v18
	v_add_f32_e32 v74, 1.0, v20
	v_exp_f32_e32 v22, v22
	v_add_f32_e32 v75, 1.0, v24
	v_exp_f32_e32 v26, v26
	v_exp_f32_e32 v30, v30
	v_mfma_f32_32x32x16_bf16 v[2:17], v[70:73], v[170:173], v[2:17]
	v_add_f32_e32 v70, 1.0, v28
	v_add_f32_e32 v71, 1.0, v32
	v_exp_f32_e32 v19, v19
	v_fmac_f32_e32 v74, v18, v74
	v_exp_f32_e32 v18, v23
	v_fmac_f32_e32 v75, v22, v75
	v_exp_f32_e32 v22, v27
	v_exp_f32_e32 v23, v31
	v_mfma_f32_32x32x16_bf16 v[2:17], v[66:69], v[166:169], v[2:17]
	v_fmac_f32_e32 v70, v26, v70
	v_fmac_f32_e32 v71, v30, v71
	v_mov_b32_e32 v27, 0xc038aa3b
	v_add_f32_e32 v19, 1.0, v19
	v_rcp_f32_e32 v26, v74
	v_rcp_f32_e32 v30, v75
	v_rcp_f32_e32 v31, v70
	v_rcp_f32_e32 v66, v71
	v_mfma_f32_32x32x16_bf16 v[2:17], v[62:65], v[162:165], v[2:17]
	v_fmamk_f32 v20, v20, 0x4038aa3b, v27
	v_add_f32_e32 v18, 1.0, v18
	v_fmamk_f32 v24, v24, 0x4038aa3b, v27
	v_add_f32_e32 v22, 1.0, v22
	v_fmamk_f32 v28, v28, 0x4038aa3b, v27
	v_rcp_f32_e32 v19, v19
	v_rcp_f32_e32 v18, v18
	v_exp_f32_e32 v21, v21
	v_exp_f32_e32 v25, v25
	v_mfma_f32_32x32x16_bf16 v[2:17], v[58:61], v[158:161], v[2:17]
	v_add_f32_e32 v23, 1.0, v23
	v_fmamk_f32 v32, v32, 0x4038aa3b, v27
	v_mul_f32_e32 v20, v20, v26
	v_mul_f32_e32 v24, v24, v30
	v_rcp_f32_e32 v22, v22
	v_rcp_f32_e32 v23, v23
	v_exp_f32_e32 v26, v29
	v_exp_f32_e32 v29, v33
	v_mfma_f32_32x32x16_bf16 v[2:17], v[54:57], v[154:157], v[2:17]
	v_mul_f32_e32 v28, v28, v31
	v_mul_f32_e32 v30, v32, v66
	v_fmac_f32_e32 v20, v19, v201
	v_fmac_f32_e32 v24, v18, v200
	v_fmac_f32_e32 v28, v22, v199
	v_fmac_f32_e32 v30, v23, v198
	v_mfma_f32_32x32x16_bf16 v[2:17], v[50:53], v[142:145], v[2:17]
	v_add_f32_e32 v18, 1.0, v21
	v_exp_f32_e32 v19, v20
	v_add_f32_e32 v20, 1.0, v25
	v_exp_f32_e32 v21, v24
	v_exp_f32_e32 v22, v28
	v_exp_f32_e32 v23, v30
	v_mfma_f32_32x32x16_bf16 v[2:17], v[46:49], v[130:133], v[2:17]
	v_add_f32_e32 v24, 1.0, v26
	v_add_f32_e32 v25, 1.0, v29
	v_fmac_f32_e32 v18, v18, v19
	v_fmac_f32_e32 v20, v20, v21
	v_fmac_f32_e32 v24, v24, v22
	v_fmac_f32_e32 v25, v25, v23
	v_mfma_f32_32x32x16_bf16 v[2:17], v[42:45], v[134:137], v[2:17]
	v_rcp_f32_e32 v18, v18
	v_rcp_f32_e32 v20, v20
	v_rcp_f32_e32 v24, v24
	v_rcp_f32_e32 v25, v25
	v_mfma_f32_32x32x16_bf16 v[2:17], v[38:41], v[138:141], v[2:17]
	v_fma_f32 v18, -v19, v18, v18
	v_fma_f32 v19, -v21, v20, v20
	v_fma_f32 v20, -v22, v24, v24
	v_fma_f32 v21, -v23, v25, v25
	v_mfma_f32_32x32x16_bf16 v[2:17], v[34:37], v[146:149], v[2:17]
	v_cvt_pk_bf16_f32 v18, v18, v19
	v_cvt_pk_bf16_f32 v19, v20, v21
	ds_write_b64 v211, v[18:19] offset:8192
	s_nop 9
	v_exp_f32_e32 v4, v4
	v_exp_f32_e32 v8, v8
	v_exp_f32_e32 v12, v12
	v_exp_f32_e32 v16, v16
	v_exp_f32_e32 v2, v2
	v_add_f32_e32 v18, 1.0, v4
	v_exp_f32_e32 v6, v6
	v_exp_f32_e32 v10, v10
	v_exp_f32_e32 v14, v14
	v_add_f32_e32 v19, 1.0, v8
	v_add_f32_e32 v20, 1.0, v12
	v_add_f32_e32 v21, 1.0, v16
	v_exp_f32_e32 v3, v3
	v_fmac_f32_e32 v18, v2, v18
	v_exp_f32_e32 v2, v7
	v_exp_f32_e32 v7, v11
	v_exp_f32_e32 v11, v15
	v_fmac_f32_e32 v19, v6, v19
	v_fmac_f32_e32 v20, v10, v20
	v_fmac_f32_e32 v21, v14, v21
	v_add_f32_e32 v3, 1.0, v3
	v_rcp_f32_e32 v6, v18
	v_rcp_f32_e32 v10, v19
	v_rcp_f32_e32 v14, v20
	v_rcp_f32_e32 v15, v21
	v_fmamk_f32 v4, v4, 0x4038aa3b, v27
	v_add_f32_e32 v2, 1.0, v2
	v_fmamk_f32 v8, v8, 0x4038aa3b, v27
	v_add_f32_e32 v7, 1.0, v7
	v_rcp_f32_e32 v3, v3
	v_rcp_f32_e32 v2, v2
	v_exp_f32_e32 v5, v5
	v_exp_f32_e32 v9, v9
	v_fmamk_f32 v12, v12, 0x4038aa3b, v27
	v_add_f32_e32 v11, 1.0, v11
	v_fmac_f32_e32 v27, 0x4038aa3b, v16
	v_mul_f32_e32 v4, v4, v6
	v_rcp_f32_e32 v6, v7
	v_rcp_f32_e32 v7, v11
	v_exp_f32_e32 v11, v13
	v_exp_f32_e32 v13, v17
	v_mul_f32_e32 v8, v8, v10
	v_mul_f32_e32 v10, v12, v14
	v_mul_f32_e32 v12, v27, v15
	v_fmac_f32_e32 v4, v3, v207
	v_fmac_f32_e32 v8, v2, v206
	v_fmac_f32_e32 v10, v6, v209
	v_fmac_f32_e32 v12, v7, v208
	v_add_f32_e32 v2, 1.0, v5
	v_exp_f32_e32 v3, v4
	v_exp_f32_e32 v4, v8
	v_exp_f32_e32 v5, v10
	v_exp_f32_e32 v6, v12
	v_add_f32_e32 v7, 1.0, v9
	v_add_f32_e32 v8, 1.0, v11
	v_add_f32_e32 v9, 1.0, v13
	v_fmac_f32_e32 v2, v2, v3
	v_fmac_f32_e32 v7, v7, v4
	v_fmac_f32_e32 v8, v8, v5
	v_fmac_f32_e32 v9, v9, v6
	v_rcp_f32_e32 v2, v2
	v_rcp_f32_e32 v7, v7
	v_rcp_f32_e32 v8, v8
	v_rcp_f32_e32 v9, v9
	v_fma_f32 v2, -v3, v2, v2
	v_fma_f32 v3, -v4, v7, v7
	v_fma_f32 v4, -v5, v8, v8
	v_fma_f32 v5, -v6, v9, v9
	v_cvt_pk_bf16_f32 v2, v2, v3
	v_cvt_pk_bf16_f32 v3, v4, v5
	ds_write_b64 v211, v[2:3] offset:8200
	s_waitcnt lgkmcnt(0)
	s_barrier
